# P3 projection output stores marked non-temporal (sc1 nt) so the 252 MB PROJ stream does not evict the GEMM operands from the memory-side cache
# speedup vs baseline: 1.0061x; 1.0004x over previous
; __device__ __forceinline__ float shx(float v, int o, int lane) { return __builtin_bit_cast(float, __builtin_amdgcn_ds_bpermute((lane ^ o) << 2, __builtin_bit_cast(int, v))); }
; __device__ __forceinline__ int fresh_lane() { int l; asm volatile("v_mbcnt_lo_u32_b32 %0, -1, 0\n\tv_mbcnt_hi_u32_b32 %0, -1, %0" : "=v"(l)); return l; }
; __device__ __forceinline__ void rows_rstd(const float* ssp, int row0, int fq, int ln, float (&rs)[8]) {
;     f32x4 a[8], b[8];
; #pragma unroll
;     for (int q = 0; q < 8; ++q) { const f32x4* p = (const f32x4*)(ssp + (size_t)(row0 + (q >> 2) * 128 + (q & 3) * 16) * 32 + 8 * fq); a[q] = p[0]; b[q] = p[1]; }
; #pragma unroll
;     for (int q = 0; q < 8; ++q) { float s = ((a[q].x + a[q].y) + (a[q].z + a[q].w)) + ((b[q].x + b[q].y) + (b[q].z + b[q].w));
;         s += shx(s, 16, ln); s += shx(s, 32, ln); rs[q] = rsqrtf(s * (1.0f / D) + RMS_EPS); }
; }
;     __device__ __forceinline__ void operator()(AccRef acc, const Unit& u, int wr, int wc, int, int) const {
;         const int ln_ = fresh_lane(), fr = ln_ & 15, fq = ln_ >> 4;
;         const int row0 = u.pm * 256 + wr * 64 + fr, col0 = u.pn * 256 + wc * 32 + 8 * fq;
;         const __amdgpu_buffer_rsrc_t rsrc = __builtin_amdgcn_make_buffer_rsrc((void*)O, 0, (int)((size_t)M * DINP * 2), 0x00020000);
;         float rs[8]; rows_rstd(ss, row0, fq, ln_, rs);
.LBB0_342:
	s_lshl_b32 s6, s6, 8
	v_mbcnt_lo_u32_b32 v178, -1, 0
	v_mbcnt_hi_u32_b32 v178, -1, v178
	s_add_i32 s6, s6, s38
	v_ashrrev_i32_e32 v130, 1, v178
	v_and_or_b32 v200, v178, 15, s6
	s_lshl_b32 s6, s7, 8
	v_and_b32_e32 v130, -8, v130
	s_or_b32 s6, s6, s39
	v_ashrrev_i32_e32 v131, 31, v130
	v_ashrrev_i32_e32 v201, 31, v200
	v_add_u32_e32 v209, s6, v130
	v_lshl_add_u64 v[130:131], v[130:131], 2, s[8:9]
	v_lshlrev_b64 v[132:133], 7, v[200:201]
	v_or_b32_e32 v134, 16, v200
	v_lshl_add_u64 v[132:133], v[130:131], 0, v[132:133]
	v_ashrrev_i32_e32 v135, 31, v134
	s_nop 0
	s_nop 0
	v_lshlrev_b64 v[134:135], 7, v[134:135]
	v_lshl_add_u64 v[134:135], v[130:131], 0, v[134:135]
	s_nop 0
	s_nop 0
	v_or_b32_e32 v134, 32, v200
	v_ashrrev_i32_e32 v135, 31, v134
	v_lshlrev_b64 v[134:135], 7, v[134:135]
	v_lshl_add_u64 v[134:135], v[130:131], 0, v[134:135]
	s_nop 0
	s_nop 0
	v_or_b32_e32 v134, 48, v200
	v_ashrrev_i32_e32 v135, 31, v134
	v_lshlrev_b64 v[134:135], 7, v[134:135]
	v_lshl_add_u64 v[130:131], v[130:131], 0, v[134:135]
	s_nop 0
	s_nop 0
	v_add_co_u32_e32 v134, vcc, s71, v132
	v_lshl_add_u64 v[130:131], v[132:133], 0, s[92:93]
	s_nop 0
	v_addc_co_u32_e32 v135, vcc, 0, v133, vcc
	v_add_co_u32_e32 v136, vcc, s72, v132
	s_mov_b64 s[6:7], 0x5000
	s_nop 0
	v_addc_co_u32_e32 v137, vcc, 0, v133, vcc
	s_nop 0
	s_nop 0
	v_lshl_add_u64 v[130:131], v[132:133], 0, s[94:95]
	s_nop 0
	s_nop 0
	v_lshl_add_u64 v[130:131], v[132:133], 0, s[6:7]
	s_nop 0
	s_nop 0
	s_mov_b64 s[6:7], 0x5800
	v_lshl_add_u64 v[130:131], v[132:133], 0, s[6:7]
	s_nop 0
	s_nop 0
	s_nop 0
	v_lshlrev_b32_e32 v178, 2, v178
	v_xor_b32_e32 v224, 64, v178
	v_xor_b32_e32 v201, 0x80, v178
	s_mov_b32 s6, 0x358637bd
	v_mov_b64_e32 v[206:207], s[6:7]
	s_mov_b32 s20, 0x3a000000
	s_mov_b32 s13, 0x800000
	s_nop 0
	v_mov_b32_e32 v178, v226
	v_mov_b32_e32 v179, v230
	v_mov_b32_e32 v230, v227
	v_mov_b32_e32 v180, v228
	v_mov_b32_e32 v181, v232
	v_mov_b32_e32 v232, v229
	v_pk_add_f32 v[178:179], v[178:179], v[230:231]
	v_pk_add_f32 v[180:181], v[180:181], v[232:233]
	v_mov_b32_e32 v182, v236
	v_pk_add_f32 v[178:179], v[178:179], v[180:181]
	v_mov_b32_e32 v180, v234
	v_mov_b32_e32 v181, v238
	v_mov_b32_e32 v238, v235
	v_mov_b32_e32 v183, v240
	v_mov_b32_e32 v240, v237
	v_pk_add_f32 v[180:181], v[180:181], v[238:239]
	v_pk_add_f32 v[182:183], v[182:183], v[240:241]
	s_nop 0
	v_pk_add_f32 v[180:181], v[180:181], v[182:183]
	v_mov_b32_e32 v183, v178
	v_mov_b32_e32 v182, v180
	v_mov_b32_e32 v178, v181
	v_pk_add_f32 v[178:179], v[182:183], v[178:179]
	ds_bpermute_b32 v181, v224, v179
	ds_bpermute_b32 v180, v224, v178
	s_waitcnt lgkmcnt(0)
	v_pk_add_f32 v[178:179], v[178:179], v[180:181]
	ds_bpermute_b32 v181, v201, v179
	ds_bpermute_b32 v180, v201, v178
	s_waitcnt lgkmcnt(0)
	v_pk_add_f32 v[178:179], v[178:179], v[180:181]
	s_nop 0
	v_pk_fma_f32 v[178:179], v[178:179], s[20:21], v[206:207] op_sel_hi:[1,0,0]
	s_nop 0
	v_mul_f32_e32 v180, 0x4b800000, v179
	v_cmp_gt_f32_e64 s[6:7], s13, v179
	v_cmp_gt_f32_e32 vcc, s13, v178
	s_nop 0
	v_cndmask_b32_e64 v179, v179, v180, s[6:7]
	v_rsq_f32_e32 v179, v179
	s_nop 0
	v_mul_f32_e32 v180, 0x45800000, v179
	v_cndmask_b32_e64 v204, v179, v180, s[6:7]
	v_mov_b32_e32 v204, v242
	v_mul_f32_e32 v179, 0x4b800000, v178
	v_cndmask_b32_e32 v178, v178, v179, vcc
	v_rsq_f32_e32 v178, v178
	v_pk_mul_f32 v[128:129], v[128:129], v[204:205] op_sel_hi:[1,0]
	v_pk_mul_f32 v[126:127], v[126:127], v[204:205] op_sel_hi:[1,0]
	v_pk_mul_f32 v[120:121], v[120:121], v[204:205] op_sel_hi:[1,0]
	v_mul_f32_e32 v179, 0x45800000, v178
	v_cndmask_b32_e32 v202, v178, v179, vcc
	v_mov_b32_e32 v202, v243
	v_mov_b32_e32 v178, v170
	v_mov_b32_e32 v179, v174
	v_mov_b32_e32 v174, v171
	v_pk_add_f32 v[170:171], v[178:179], v[174:175]
	v_mov_b32_e32 v174, v172
	v_mov_b32_e32 v175, v176
	v_mov_b32_e32 v176, v173
	v_pk_add_f32 v[172:173], v[174:175], v[176:177]
	v_pk_mul_f32 v[118:119], v[118:119], v[204:205] op_sel_hi:[1,0]
	v_pk_add_f32 v[170:171], v[170:171], v[172:173]
	v_mov_b32_e32 v172, v166
	v_mov_b32_e32 v173, v162
	v_mov_b32_e32 v162, v167
	v_mov_b32_e32 v166, v168
	v_mov_b32_e32 v167, v164
	v_mov_b32_e32 v164, v169
	v_pk_add_f32 v[162:163], v[172:173], v[162:163]
	v_pk_add_f32 v[164:165], v[166:167], v[164:165]
	v_mov_b32_e32 v166, v158
	v_pk_add_f32 v[162:163], v[162:163], v[164:165]
	v_mov_b32_e32 v165, v170
	v_mov_b32_e32 v164, v162
	v_mov_b32_e32 v170, v163
	v_pk_add_f32 v[162:163], v[164:165], v[170:171]
	ds_bpermute_b32 v165, v224, v163
	ds_bpermute_b32 v164, v224, v162
	v_mov_b32_e32 v167, v154
	v_mov_b32_e32 v154, v159
	v_mov_b32_e32 v158, v160
	v_mov_b32_e32 v159, v156
	v_mov_b32_e32 v156, v161
	v_pk_add_f32 v[154:155], v[166:167], v[154:155]
	v_pk_add_f32 v[156:157], v[158:159], v[156:157]
	s_waitcnt lgkmcnt(0)
	v_pk_add_f32 v[162:163], v[162:163], v[164:165]
	v_pk_add_f32 v[154:155], v[154:155], v[156:157]
	v_mov_b32_e32 v156, v150
	v_mov_b32_e32 v157, v146
	v_mov_b32_e32 v146, v151
	v_mov_b32_e32 v150, v152
	v_mov_b32_e32 v151, v148
	v_mov_b32_e32 v148, v153
	v_pk_add_f32 v[146:147], v[156:157], v[146:147]
	v_pk_add_f32 v[148:149], v[150:151], v[148:149]
	ds_bpermute_b32 v165, v201, v163
	v_pk_add_f32 v[146:147], v[146:147], v[148:149]
	v_mov_b32_e32 v149, v154
	v_mov_b32_e32 v148, v146
	v_mov_b32_e32 v154, v147
	ds_bpermute_b32 v164, v201, v162
	v_pk_add_f32 v[146:147], v[148:149], v[154:155]
	ds_bpermute_b32 v149, v224, v147
	ds_bpermute_b32 v148, v224, v146
	v_mov_b32_e32 v150, v142
	v_mov_b32_e32 v151, v138
	v_mov_b32_e32 v138, v143
	v_mov_b32_e32 v142, v144
	v_mov_b32_e32 v143, v140
	v_mov_b32_e32 v140, v145
	v_pk_add_f32 v[138:139], v[150:151], v[138:139]
	v_pk_add_f32 v[140:141], v[142:143], v[140:141]
	s_waitcnt lgkmcnt(2)
; __device__ __forceinline__ unsigned cvt_pk_bf16(float lo, float hi) { unsigned r; asm volatile("v_cvt_pk_bf16_f32 %0, %1, %2" : "=v"(r) : "v"(lo), "v"(hi)); return r; }
; __device__ __forceinline__ void store16_wt(__amdgpu_buffer_rsrc_t rsrc, unsigned byte_off, v4u v) { __builtin_amdgcn_raw_buffer_store_b128(v, rsrc, byte_off, 0, 16); }
;     __device__ __forceinline__ void operator()(AccRef acc, const Unit& u, int wr, int wc, int, int) const {
;     ...
;         for (int ai = 0; ai < 2; ++ai)
; #pragma unroll
;             for (int m = 0; m < 4; ++m) {
;                 const int row = row0 + ai * 128 + m * 16;
;                 const float r = rs[ai * 4 + m];
; #pragma unroll
;                 for (int bj = 0; bj < 2; ++bj) {
;                     const f32x4 v0 = acc[ai][bj][m][0] * r, v1 = acc[ai][bj][m][1] * r;
;                     v4u w; w.x = cvt_pk_bf16(v0[0], v0[1]); w.y = cvt_pk_bf16(v0[2], v0[3]); w.z = cvt_pk_bf16(v1[0], v1[1]); w.w = cvt_pk_bf16(v1[2], v1[3]);
;                     store16_wt(rsrc, (unsigned)(((size_t)row * DINP + col0 + bj * 128) * 2), w);
;                 }
	v_pk_add_f32 v[162:163], v[162:163], v[164:165]
	v_pk_add_f32 v[138:139], v[138:139], v[140:141]
	v_mov_b32_e32 v140, v134
	v_mov_b32_e32 v141, v130
	v_mov_b32_e32 v130, v135
	v_mov_b32_e32 v134, v136
	v_mov_b32_e32 v135, v132
	v_mov_b32_e32 v132, v137
	v_pk_add_f32 v[130:131], v[140:141], v[130:131]
	v_pk_add_f32 v[132:133], v[134:135], v[132:133]
	v_pk_fma_f32 v[162:163], v[162:163], s[20:21], v[206:207] op_sel_hi:[1,0,0]
	v_pk_add_f32 v[130:131], v[130:131], v[132:133]
	s_waitcnt lgkmcnt(0)
	v_pk_add_f32 v[146:147], v[146:147], v[148:149]
	v_mov_b32_e32 v132, v130
	v_mov_b32_e32 v133, v138
	v_mov_b32_e32 v138, v131
	v_mul_f32_e32 v164, 0x4b800000, v163
	v_cmp_gt_f32_e64 s[6:7], s13, v163
	ds_bpermute_b32 v149, v201, v147
	ds_bpermute_b32 v148, v201, v146
	v_pk_add_f32 v[130:131], v[132:133], v[138:139]
	v_cndmask_b32_e64 v163, v163, v164, s[6:7]
	ds_bpermute_b32 v133, v224, v131
	ds_bpermute_b32 v132, v224, v130
	v_rsq_f32_e32 v163, v163
	s_waitcnt lgkmcnt(2)
	v_pk_add_f32 v[146:147], v[146:147], v[148:149]
	v_cmp_gt_f32_e32 vcc, s13, v162
	v_pk_fma_f32 v[146:147], v[146:147], s[20:21], v[206:207] op_sel_hi:[1,0,0]
	v_mul_f32_e32 v164, 0x45800000, v163
	s_waitcnt lgkmcnt(0)
	v_pk_add_f32 v[130:131], v[130:131], v[132:133]
	v_cndmask_b32_e64 v164, v163, v164, s[6:7]
	v_mov_b32_e32 v164, v244
	v_mul_f32_e32 v163, 0x4b800000, v162
	v_mul_f32_e32 v148, 0x4b800000, v147
	v_cmp_gt_f32_e64 s[6:7], s13, v147
	ds_bpermute_b32 v133, v201, v131
	ds_bpermute_b32 v132, v201, v130
	v_cndmask_b32_e32 v162, v162, v163, vcc
	v_cndmask_b32_e64 v147, v147, v148, s[6:7]
	v_rsq_f32_e32 v162, v162
	v_rsq_f32_e32 v147, v147
	s_waitcnt lgkmcnt(0)
	v_pk_add_f32 v[130:131], v[130:131], v[132:133]
	v_pk_mul_f32 v[134:135], v[124:125], v[204:205] op_sel_hi:[1,0]
	v_mul_f32_e32 v163, 0x45800000, v162
	v_mul_f32_e32 v148, 0x45800000, v147
	v_pk_fma_f32 v[130:131], v[130:131], s[20:21], v[206:207] op_sel_hi:[1,0,0]
	v_cndmask_b32_e32 v162, v162, v163, vcc
	v_mov_b32_e32 v162, v245
	v_cmp_gt_f32_e32 vcc, s13, v146
	v_cndmask_b32_e64 v148, v147, v148, s[6:7]
	v_mov_b32_e32 v148, v246
	v_mul_f32_e32 v147, 0x4b800000, v146
	v_mul_f32_e32 v132, 0x4b800000, v131
	v_cmp_gt_f32_e64 s[6:7], s13, v131
	v_cndmask_b32_e32 v146, v146, v147, vcc
	v_rsq_f32_e32 v146, v146
	v_cndmask_b32_e64 v131, v131, v132, s[6:7]
	v_rsq_f32_e32 v131, v131
	v_readlane_b32 s20, v254, 19
	v_mul_f32_e32 v147, 0x45800000, v146
	v_cndmask_b32_e32 v146, v146, v147, vcc
	v_mov_b32_e32 v146, v247
	v_mul_f32_e32 v132, 0x45800000, v131
	v_cmp_gt_f32_e32 vcc, s13, v130
	v_cndmask_b32_e64 v132, v131, v132, s[6:7]
	v_mov_b32_e32 v132, v248
	v_mul_f32_e32 v131, 0x4b800000, v130
	v_cndmask_b32_e32 v130, v130, v131, vcc
	v_rsq_f32_e32 v130, v130
	s_movk_i32 s6, 0x3c00
	v_pk_mul_f32 v[124:125], v[122:123], v[204:205] op_sel_hi:[1,0]
	v_cvt_pk_bf16_f32 v122, v126, v127
	v_mul_f32_e32 v131, 0x45800000, v130
	v_cndmask_b32_e32 v130, v130, v131, vcc
	v_mov_b32_e32 v130, v249
	v_mul_lo_u32 v131, v200, s6
	v_add_lshl_u32 v131, v209, v131, 1
	v_cvt_pk_bf16_f32 v123, v128, v129
	v_readlane_b32 s21, v254, 20
	v_readlane_b32 s22, v254, 21
	v_readlane_b32 s23, v254, 22
	v_cvt_pk_bf16_f32 v124, v124, v125
	v_cvt_pk_bf16_f32 v125, v134, v135
	v_pk_mul_f32 v[104:105], v[104:105], v[202:203] op_sel_hi:[1,0]
	v_pk_mul_f32 v[102:103], v[102:103], v[202:203] op_sel_hi:[1,0]
	v_pk_mul_f32 v[88:89], v[88:89], v[164:165] op_sel_hi:[1,0]
	s_nop 1
	buffer_store_dwordx4 v[122:125], v131, s[20:23], 0 offen sc1 nt
	v_pk_mul_f32 v[86:87], v[86:87], v[164:165] op_sel_hi:[1,0]
	v_pk_mul_f32 v[72:73], v[72:73], v[162:163] op_sel_hi:[1,0]
	v_pk_mul_f32 v[122:123], v[112:113], v[204:205] op_sel_hi:[1,0]
	v_pk_mul_f32 v[112:113], v[110:111], v[204:205] op_sel_hi:[1,0]
	v_cvt_pk_bf16_f32 v110, v118, v119
	v_cvt_pk_bf16_f32 v111, v120, v121
	v_add_u32_e32 v118, 0x78000, v131
	v_cvt_pk_bf16_f32 v112, v112, v113
	v_cvt_pk_bf16_f32 v113, v122, v123
	buffer_store_dwordx4 v[110:113], v131, s[20:23], 0 offen offset:256 sc1 nt
	v_pk_mul_f32 v[70:71], v[70:71], v[162:163] op_sel_hi:[1,0]
	v_pk_mul_f32 v[64:65], v[64:65], v[148:149] op_sel_hi:[1,0]
	v_pk_mul_f32 v[110:111], v[116:117], v[202:203] op_sel_hi:[1,0]
	v_pk_mul_f32 v[112:113], v[114:115], v[202:203] op_sel_hi:[1,0]
	v_pk_mul_f32 v[114:115], v[108:109], v[202:203] op_sel_hi:[1,0]
	v_pk_mul_f32 v[108:109], v[106:107], v[202:203] op_sel_hi:[1,0]
	v_cvt_pk_bf16_f32 v106, v112, v113
	v_cvt_pk_bf16_f32 v107, v110, v111
	v_pk_mul_f32 v[62:63], v[62:63], v[148:149] op_sel_hi:[1,0]
	v_cvt_pk_bf16_f32 v108, v108, v109
	v_cvt_pk_bf16_f32 v109, v114, v115
	buffer_store_dwordx4 v[106:109], v118, s[20:23], 0 offen sc1 nt
	v_pk_mul_f32 v[56:57], v[56:57], v[148:149] op_sel_hi:[1,0]
	v_pk_mul_f32 v[54:55], v[54:55], v[148:149] op_sel_hi:[1,0]
	v_pk_mul_f32 v[106:107], v[96:97], v[202:203] op_sel_hi:[1,0]
	v_pk_mul_f32 v[96:97], v[94:95], v[202:203] op_sel_hi:[1,0]
	v_cvt_pk_bf16_f32 v94, v102, v103
	v_cvt_pk_bf16_f32 v95, v104, v105
	v_add_u32_e32 v102, 0xf0000, v131
	v_cvt_pk_bf16_f32 v96, v96, v97
	v_cvt_pk_bf16_f32 v97, v106, v107
	buffer_store_dwordx4 v[94:97], v118, s[20:23], 0 offen offset:256 sc1 nt
	v_pk_mul_f32 v[40:41], v[40:41], v[146:147] op_sel_hi:[1,0]
; __device__ __forceinline__ unsigned cvt_pk_bf16(float lo, float hi) { unsigned r; asm volatile("v_cvt_pk_bf16_f32 %0, %1, %2" : "=v"(r) : "v"(lo), "v"(hi)); return r; }
; #define PG8_BAR __builtin_amdgcn_s_barrier()
; __device__ __forceinline__ void store16_wt(__amdgpu_buffer_rsrc_t rsrc, unsigned byte_off, v4u v) { __builtin_amdgcn_raw_buffer_store_b128(v, rsrc, byte_off, 0, 16); }
; template <class Epi, class Sched, bool ALIGN_EPI = false, bool SP2 = false>
; __device__ __forceinline__ void gemm_phase(PG8_LAS unsigned char* lds, const Gemm g, const Sched& S, const Epi& E, int tid_) {
;     ...
;         if constexpr (ALIGN_EPI) { if (wr == 0) PG8_BAR; }
;         E(acc, cur, wr, wc, fr, fq); S.done(cur);
;         if (!has_next) break;
;         if (!(Epi::KEEP && E.keep(cur))) {
; #pragma unroll
;         for (int a = 0; a < 2; ++a)
; #pragma unroll
;             for (int b = 0; b < 2; ++b)
; #pragma unroll
;                 for (int m = 0; m < 4; ++m)
; #pragma unroll
;                     for (int n = 0; n < 2; ++n) acc[a][b][m][n] = (f32x4){0.f, 0.f, 0.f, 0.f};
;         }
;         cur = nxt; cA = nA; cB = nB; ++ui;
;         if constexpr (ALIGN_EPI) { if (wr == 1) PG8_BAR; }
;     }
;     __device__ __forceinline__ void operator()(AccRef acc, const Unit& u, int wr, int wc, int, int) const {
;     ...
;         for (int ai = 0; ai < 2; ++ai)
; #pragma unroll
;             for (int m = 0; m < 4; ++m) {
;                 const int row = row0 + ai * 128 + m * 16;
;                 const float r = rs[ai * 4 + m];
; #pragma unroll
;                 for (int bj = 0; bj < 2; ++bj) {
;                     const f32x4 v0 = acc[ai][bj][m][0] * r, v1 = acc[ai][bj][m][1] * r;
;                     v4u w; w.x = cvt_pk_bf16(v0[0], v0[1]); w.y = cvt_pk_bf16(v0[2], v0[3]); w.z = cvt_pk_bf16(v1[0], v1[1]); w.w = cvt_pk_bf16(v1[2], v1[3]);
;                     store16_wt(rsrc, (unsigned)(((size_t)row * DINP + col0 + bj * 128) * 2), w);
;                 }
	v_pk_mul_f32 v[38:39], v[38:39], v[146:147] op_sel_hi:[1,0]
	v_pk_mul_f32 v[94:95], v[100:101], v[164:165] op_sel_hi:[1,0]
	v_pk_mul_f32 v[96:97], v[98:99], v[164:165] op_sel_hi:[1,0]
	v_pk_mul_f32 v[98:99], v[92:93], v[164:165] op_sel_hi:[1,0]
	v_pk_mul_f32 v[92:93], v[90:91], v[164:165] op_sel_hi:[1,0]
	v_cvt_pk_bf16_f32 v90, v96, v97
	v_cvt_pk_bf16_f32 v91, v94, v95
	v_pk_mul_f32 v[24:25], v[24:25], v[132:133] op_sel_hi:[1,0]
	v_cvt_pk_bf16_f32 v92, v92, v93
	v_cvt_pk_bf16_f32 v93, v98, v99
	buffer_store_dwordx4 v[90:93], v102, s[20:23], 0 offen sc1 nt
	v_pk_mul_f32 v[22:23], v[22:23], v[132:133] op_sel_hi:[1,0]
	s_mov_b64 s[6:7], -1
	v_pk_mul_f32 v[90:91], v[80:81], v[164:165] op_sel_hi:[1,0]
	v_pk_mul_f32 v[80:81], v[78:79], v[164:165] op_sel_hi:[1,0]
	v_cvt_pk_bf16_f32 v78, v86, v87
	v_cvt_pk_bf16_f32 v79, v88, v89
	v_add_u32_e32 v86, 0x168000, v131
	v_cvt_pk_bf16_f32 v80, v80, v81
	v_cvt_pk_bf16_f32 v81, v90, v91
	buffer_store_dwordx4 v[78:81], v102, s[20:23], 0 offen offset:256 sc1 nt
	s_andn2_b64 vcc, exec, s[4:5]
	v_pk_mul_f32 v[6:7], v[6:7], v[130:131] op_sel_hi:[1,0]
	v_pk_mul_f32 v[78:79], v[84:85], v[162:163] op_sel_hi:[1,0]
	v_pk_mul_f32 v[80:81], v[82:83], v[162:163] op_sel_hi:[1,0]
	v_pk_mul_f32 v[82:83], v[76:77], v[162:163] op_sel_hi:[1,0]
	v_pk_mul_f32 v[76:77], v[74:75], v[162:163] op_sel_hi:[1,0]
	v_cvt_pk_bf16_f32 v74, v80, v81
	v_cvt_pk_bf16_f32 v75, v78, v79
	v_pk_mul_f32 v[4:5], v[4:5], v[130:131] op_sel_hi:[1,0]
	v_cvt_pk_bf16_f32 v76, v76, v77
	v_cvt_pk_bf16_f32 v77, v82, v83
	buffer_store_dwordx4 v[74:77], v86, s[20:23], 0 offen sc1 nt
	s_nop 1
	v_pk_mul_f32 v[74:75], v[68:69], v[162:163] op_sel_hi:[1,0]
	v_pk_mul_f32 v[68:69], v[66:67], v[162:163] op_sel_hi:[1,0]
	v_cvt_pk_bf16_f32 v66, v70, v71
	v_cvt_pk_bf16_f32 v67, v72, v73
	s_nop 0
	v_cvt_pk_bf16_f32 v68, v68, v69
	v_cvt_pk_bf16_f32 v69, v74, v75
	buffer_store_dwordx4 v[66:69], v86, s[20:23], 0 offen offset:256 sc1 nt
	s_nop 1
	v_add_u32_e32 v68, 0x3c0000, v131
	v_pk_mul_f32 v[66:67], v[60:61], v[148:149] op_sel_hi:[1,0]
	v_pk_mul_f32 v[60:61], v[58:59], v[148:149] op_sel_hi:[1,0]
	v_cvt_pk_bf16_f32 v58, v62, v63
	v_cvt_pk_bf16_f32 v59, v64, v65
	s_nop 0
	v_cvt_pk_bf16_f32 v60, v60, v61
	v_cvt_pk_bf16_f32 v61, v66, v67
	buffer_store_dwordx4 v[58:61], v68, s[20:23], 0 offen sc1 nt
	s_nop 1
	v_pk_mul_f32 v[58:59], v[48:49], v[148:149] op_sel_hi:[1,0]
	v_pk_mul_f32 v[48:49], v[46:47], v[148:149] op_sel_hi:[1,0]
	v_cvt_pk_bf16_f32 v46, v54, v55
	v_cvt_pk_bf16_f32 v47, v56, v57
	v_add_u32_e32 v54, 0x438000, v131
	v_cvt_pk_bf16_f32 v48, v48, v49
	v_cvt_pk_bf16_f32 v49, v58, v59
	buffer_store_dwordx4 v[46:49], v68, s[20:23], 0 offen offset:256 sc1 nt
	s_nop 1
	v_pk_mul_f32 v[46:47], v[52:53], v[146:147] op_sel_hi:[1,0]
	v_pk_mul_f32 v[48:49], v[50:51], v[146:147] op_sel_hi:[1,0]
	v_pk_mul_f32 v[50:51], v[44:45], v[146:147] op_sel_hi:[1,0]
	v_pk_mul_f32 v[44:45], v[42:43], v[146:147] op_sel_hi:[1,0]
	v_cvt_pk_bf16_f32 v42, v48, v49
	v_cvt_pk_bf16_f32 v43, v46, v47
	s_nop 0
	v_cvt_pk_bf16_f32 v44, v44, v45
	v_cvt_pk_bf16_f32 v45, v50, v51
	buffer_store_dwordx4 v[42:45], v54, s[20:23], 0 offen sc1 nt
	s_nop 1
	v_pk_mul_f32 v[42:43], v[32:33], v[146:147] op_sel_hi:[1,0]
	v_pk_mul_f32 v[32:33], v[30:31], v[146:147] op_sel_hi:[1,0]
	v_cvt_pk_bf16_f32 v30, v38, v39
	v_cvt_pk_bf16_f32 v31, v40, v41
	v_add_u32_e32 v38, 0x4b0000, v131
	v_cvt_pk_bf16_f32 v32, v32, v33
	v_cvt_pk_bf16_f32 v33, v42, v43
	buffer_store_dwordx4 v[30:33], v54, s[20:23], 0 offen offset:256 sc1 nt
	s_nop 1
	v_pk_mul_f32 v[30:31], v[36:37], v[132:133] op_sel_hi:[1,0]
	v_pk_mul_f32 v[32:33], v[34:35], v[132:133] op_sel_hi:[1,0]
	v_pk_mul_f32 v[34:35], v[28:29], v[132:133] op_sel_hi:[1,0]
	v_pk_mul_f32 v[28:29], v[26:27], v[132:133] op_sel_hi:[1,0]
	v_cvt_pk_bf16_f32 v26, v32, v33
	v_cvt_pk_bf16_f32 v27, v30, v31
	s_nop 0
	v_cvt_pk_bf16_f32 v28, v28, v29
	v_cvt_pk_bf16_f32 v29, v34, v35
	buffer_store_dwordx4 v[26:29], v38, s[20:23], 0 offen sc1 nt
	s_nop 1
	v_pk_mul_f32 v[26:27], v[16:17], v[132:133] op_sel_hi:[1,0]
	v_pk_mul_f32 v[16:17], v[14:15], v[132:133] op_sel_hi:[1,0]
	v_cvt_pk_bf16_f32 v14, v22, v23
	v_cvt_pk_bf16_f32 v15, v24, v25
	v_add_u32_e32 v22, 0x528000, v131
	v_cvt_pk_bf16_f32 v16, v16, v17
	v_cvt_pk_bf16_f32 v17, v26, v27
	buffer_store_dwordx4 v[14:17], v38, s[20:23], 0 offen offset:256 sc1 nt
	s_nop 1
	v_pk_mul_f32 v[14:15], v[20:21], v[130:131] op_sel_hi:[1,0]
	v_pk_mul_f32 v[16:17], v[18:19], v[130:131] op_sel_hi:[1,0]
	v_pk_mul_f32 v[18:19], v[12:13], v[130:131] op_sel_hi:[1,0]
	v_pk_mul_f32 v[12:13], v[10:11], v[130:131] op_sel_hi:[1,0]
	v_cvt_pk_bf16_f32 v10, v16, v17
	v_cvt_pk_bf16_f32 v11, v14, v15
	s_nop 0
	v_cvt_pk_bf16_f32 v12, v12, v13
	v_cvt_pk_bf16_f32 v13, v18, v19
	buffer_store_dwordx4 v[10:13], v22, s[20:23], 0 offen sc1 nt
	s_nop 1
	v_pk_mul_f32 v[10:11], v[2:3], v[130:131] op_sel_hi:[1,0]
	v_pk_mul_f32 v[2:3], v[0:1], v[130:131] op_sel_hi:[1,0]
	v_cvt_pk_bf16_f32 v0, v4, v5
	v_cvt_pk_bf16_f32 v1, v6, v7
	s_nop 0
	v_cvt_pk_bf16_f32 v2, v2, v3
	v_cvt_pk_bf16_f32 v3, v10, v11
	buffer_store_dwordx4 v[0:3], v22, s[20:23], 0 offen offset:256 sc1 nt
	s_cbranch_vccnz .LBB0_335
	s_andn2_b64 vcc, exec, s[0:1]
	s_cbranch_vccnz .LBB0_334
	s_barrier
	s_branch .LBB0_334
